# output waves prefetch next iteration's f32 z rows from LDS mid-iteration so the row output starts right after the barrier
# speedup vs baseline: 1.0180x; 1.0180x over previous
.LBB0_88:
	s_add_i32 s29, s17, -1
	s_and_b32 s0, s29, 1
	s_mulk_i32 s0, 0x1200
	v_add_u32_e32 v254, s0, v185
	ds_read_b128 v[250:253], v254
	ds_read_b128 v[194:197], v179
	ds_read_b128 v[198:201], v179 offset:32
	ds_read_b128 v[202:205], v179 offset:64
	ds_read_b128 v[206:209], v179 offset:96
	s_cmp_lt_u32 s17, 2
	s_cbranch_scc1 .Low_noout
	v_cmp_lt_i32_e64 s[0:1], -1, v192
	s_waitcnt vmcnt(0)
	s_and_saveexec_b64 s[6:7], s[0:1]
	s_cbranch_execz .Low_a_donel
	v_pk_add_f32 v[66:67], v[246:247], v[224:225] neg_lo:[0,1] neg_hi:[0,1]
	v_pk_add_f32 v[74:75], v[248:249], v[226:227] neg_lo:[0,1] neg_hi:[0,1]
	v_pk_fma_f32 v[222:223], v[66:67], v[66:67], v[222:223]
	v_pk_fma_f32 v[222:223], v[74:75], v[74:75], v[222:223]
	v_pk_add_f32 v[66:67], v[224:225], v[66:67]
	v_pk_add_f32 v[68:69], v[226:227], v[74:75]
	global_store_dwordx4 v[168:169], v[66:69], off sc0 sc1
	s_nop 1
.Low_a_donel:
	s_or_b64 exec, exec, s[6:7]
	v_cmp_lt_i32_e64 s[0:1], -1, v191
	s_and_saveexec_b64 s[6:7], s[0:1]
	s_cbranch_execz .Low_b_donel
	v_pk_add_f32 v[70:71], v[162:163], v[228:229] neg_lo:[0,1] neg_hi:[0,1]
	v_pk_add_f32 v[72:73], v[164:165], v[230:231] neg_lo:[0,1] neg_hi:[0,1]
	v_pk_fma_f32 v[222:223], v[70:71], v[70:71], v[222:223]
	v_pk_fma_f32 v[222:223], v[72:73], v[72:73], v[222:223]
	v_pk_add_f32 v[66:67], v[228:229], v[70:71]
	v_pk_add_f32 v[68:69], v[230:231], v[72:73]
	global_store_dwordx4 v[170:171], v[66:69], off sc0 sc1
	s_nop 1

.Low_noout:
	s_waitcnt lgkmcnt(4)
	v_lshlrev_b32_e32 v210, 1, v250
	v_lshlrev_b32_e32 v211, 1, v252
	v_and_b32_e32 v212, 0xfffffc03, v250
	v_and_b32_e32 v213, 0xfffffc03, v252
	v_and_b32_e32 v210, 0x78, v210
	v_and_b32_e32 v211, 0x78, v211
	v_or3_b32 v212, v212, v210, v176
	v_or3_b32 v213, v213, v211, v187
	v_min_f32_e32 v210, v212, v213
	v_max_f32_e32 v211, v212, v213
	v_min3_f32 v211, v251, v253, v211
	v_max_f32_dpp v212, v210, v210 quad_perm:[1,0,3,2] row_mask:0xf bank_mask:0xf
	v_min_f32_dpp v213, v210, v210 quad_perm:[1,0,3,2] row_mask:0xf bank_mask:0xf
	v_mov_b32_dpp v254, v211 quad_perm:[1,0,3,2] row_mask:0xf bank_mask:0xf
	v_min3_f32 v211, v211, v254, v212
	v_max_f32_dpp v212, v213, v213 quad_perm:[2,3,0,1] row_mask:0xf bank_mask:0xf
	v_min_f32_dpp v210, v213, v213 quad_perm:[2,3,0,1] row_mask:0xf bank_mask:0xf
	v_mov_b32_dpp v254, v211 quad_perm:[2,3,0,1] row_mask:0xf bank_mask:0xf
	v_min3_f32 v211, v211, v254, v212
	v_max_f32_dpp v212, v210, v210 row_half_mirror row_mask:0xf bank_mask:0xf
	v_min_f32_dpp v213, v210, v210 row_half_mirror row_mask:0xf bank_mask:0xf
	v_mov_b32_dpp v254, v211 row_half_mirror row_mask:0xf bank_mask:0xf
	v_min3_f32 v211, v211, v254, v212
	s_and_saveexec_b64 s[6:7], vcc
	s_cbranch_execz .Low_m_done
	v_sub_f32_e32 v212, v211, v213
	v_cmp_gt_f32_e64 s[0:1], s26, v212
	s_nop 1
	v_cndmask_b32_e64 v212, 0, v190, s[0:1]
	v_and_or_b32 v212, v213, s27, v212
	ds_write_b32 v186, v212
	s_and_b64 exec, exec, s[0:1]
	s_cbranch_execz .Low_m_done
	s_mov_b64 s[14:15], exec
	v_mbcnt_lo_u32_b32 v212, s14, 0
	v_mbcnt_hi_u32_b32 v212, s15, v212
	v_cmp_eq_u32_e64 s[0:1], 0, v212
	s_and_saveexec_b64 s[8:9], s[0:1]
	s_bcnt1_i32_b64 s0, s[14:15]
	v_mov_b32_e32 v254, s0
	ds_add_rtn_u32 v254, v189, v254
	s_or_b64 exec, exec, s[8:9]
	s_waitcnt lgkmcnt(0)
	v_readfirstlane_b32 s0, v254
	v_add_f32_e32 v213, 0x3d4ccccd, v213
	s_nop 0
	v_add_lshl_u32 v212, s0, v212, 2
	v_add_u32_e32 v254, 0x21400, v212
	v_add_u32_e32 v212, 0x20400, v212
	ds_write_b32 v254, v166
	ds_write_b32 v212, v213
.Low_m_done:
	s_or_b64 exec, exec, s[6:7]
	s_waitcnt lgkmcnt(0)
	v_mfma_f32_32x32x16_f16 v[66:81], v[98:101], v[194:197], v[2:17]
	v_mfma_f32_32x32x16_f16 v[66:81], v[102:105], v[198:201], v[66:81]
	v_add_u32_e32 v254, 0x20c00, v188
	s_waitcnt lgkmcnt(0)
	ds_read_b32 v191, v254 offset:64
	ds_read_b32 v192, v254
	v_mfma_f32_32x32x16_f16 v[66:81], v[106:109], v[202:205], v[66:81]
	v_mfma_f32_32x32x16_f16 v[66:81], v[110:113], v[206:209], v[66:81]
	v_mfma_f32_32x32x16_f16 v[82:97], v[114:117], v[194:197], v[18:33]
	s_waitcnt lgkmcnt(0)
	v_and_b32_e32 v212, s27, v191
	v_lshl_or_b32 v212, v212, 8, v178
	global_load_dwordx4 v[162:165], v212, s[22:23]
	v_and_b32_e32 v213, s27, v192
	v_lshl_or_b32 v213, v213, 8, v178
	global_load_dwordx4 v[246:249], v213, s[22:23]
	s_and_b32 s1, s29, 3
	v_lshl_add_u32 v212, s1, 13, v175
	v_lshl_add_u32 v213, s1, 13, v174
	ds_read_b128 v[224:227], v212
	ds_read_b128 v[228:231], v213
	v_and_b32_e32 v66, 0xffffffc0, v66
	v_and_or_b32 v67, v67, s16, 1
	v_and_or_b32 v68, v68, s16, 2
	v_and_or_b32 v69, v69, s16, 3
	v_med3_f32 v211, v66, v67, s25
	v_and_or_b32 v70, v70, s16, 4
	v_min3_f32 v210, v66, s25, v67
	v_and_or_b32 v71, v71, s16, 5
	v_mfma_f32_32x32x16_f16 v[82:97], v[118:121], v[198:201], v[82:97]
	v_med3_f32 v214, v210, v68, v69
	v_and_or_b32 v72, v72, s16, 6
	v_min3_f32 v212, v210, v68, v69
	v_and_or_b32 v73, v73, s16, 7
	v_min3_f32 v213, v211, s25, v214
	v_med3_f32 v211, v212, v70, v71
	v_and_or_b32 v74, v74, s16, 8
	v_min3_f32 v210, v212, v70, v71
	v_mfma_f32_32x32x16_f16 v[82:97], v[122:125], v[202:205], v[82:97]
	v_and_or_b32 v75, v75, s16, 9
	v_med3_f32 v214, v210, v72, v73
	v_and_or_b32 v76, v76, s16, 10
	v_min3_f32 v212, v210, v72, v73
	v_and_or_b32 v77, v77, s16, 11
	v_min3_f32 v213, v213, v211, v214
	v_med3_f32 v211, v212, v74, v75
	v_and_or_b32 v78, v78, s16, 12
	v_mfma_f32_32x32x16_f16 v[82:97], v[126:129], v[206:209], v[82:97]
	v_min3_f32 v210, v212, v74, v75
	v_and_or_b32 v79, v79, s16, 13
	v_med3_f32 v214, v210, v76, v77
	v_and_or_b32 v80, v80, s16, 14
	v_min3_f32 v212, v210, v76, v77
	v_and_or_b32 v81, v81, s16, 15
	v_min3_f32 v213, v213, v211, v214
	v_med3_f32 v211, v212, v78, v79
	v_min3_f32 v210, v212, v78, v79
	v_med3_f32 v214, v210, v80, v81
	v_min3_f32 v212, v210, v80, v81
	v_min3_f32 v213, v213, v211, v214
	v_mfma_f32_32x32x16_f16 v[66:81], v[130:133], v[194:197], v[34:49]
	v_and_or_b32 v82, v82, s16, 16
	v_and_or_b32 v83, v83, s16, 17
	v_and_or_b32 v84, v84, s16, 18
	v_and_or_b32 v85, v85, s16, 19
	v_med3_f32 v211, v212, v82, v83
	v_and_or_b32 v86, v86, s16, 20
	v_min3_f32 v210, v212, v82, v83
	v_and_or_b32 v87, v87, s16, 21
	v_mfma_f32_32x32x16_f16 v[66:81], v[134:137], v[198:201], v[66:81]
	v_med3_f32 v214, v210, v84, v85
	v_and_or_b32 v88, v88, s16, 22
	v_min3_f32 v212, v210, v84, v85
	v_and_or_b32 v89, v89, s16, 23
	v_min3_f32 v213, v213, v211, v214
	v_med3_f32 v211, v212, v86, v87
	v_and_or_b32 v90, v90, s16, 24
	v_min3_f32 v210, v212, v86, v87
	v_mfma_f32_32x32x16_f16 v[66:81], v[138:141], v[202:205], v[66:81]
	v_and_or_b32 v91, v91, s16, 25
	v_med3_f32 v214, v210, v88, v89
	v_and_or_b32 v92, v92, s16, 26
	v_min3_f32 v212, v210, v88, v89
	v_and_or_b32 v93, v93, s16, 27
	v_min3_f32 v213, v213, v211, v214
	v_med3_f32 v211, v212, v90, v91
	v_and_or_b32 v94, v94, s16, 28
	v_mfma_f32_32x32x16_f16 v[66:81], v[142:145], v[206:209], v[66:81]
	v_min3_f32 v210, v212, v90, v91
	v_and_or_b32 v95, v95, s16, 29
	v_med3_f32 v214, v210, v92, v93
	v_and_or_b32 v96, v96, s16, 30
	v_min3_f32 v212, v210, v92, v93
	v_and_or_b32 v97, v97, s16, 31
	v_min3_f32 v213, v213, v211, v214
	v_med3_f32 v211, v212, v94, v95
	v_min3_f32 v210, v212, v94, v95
	v_med3_f32 v214, v210, v96, v97
	v_min3_f32 v212, v210, v96, v97
	v_min3_f32 v213, v213, v211, v214
	v_mfma_f32_32x32x16_f16 v[82:97], v[146:149], v[194:197], v[50:65]
	v_and_or_b32 v66, v66, s16, 32
	v_and_or_b32 v67, v67, s16, 33
	v_and_or_b32 v68, v68, s16, 34
	v_and_or_b32 v69, v69, s16, 35
	v_med3_f32 v211, v212, v66, v67
	v_and_or_b32 v70, v70, s16, 36
	v_min3_f32 v210, v212, v66, v67
	v_and_or_b32 v71, v71, s16, 37
	v_mfma_f32_32x32x16_f16 v[82:97], v[150:153], v[198:201], v[82:97]
	v_med3_f32 v214, v210, v68, v69
	v_and_or_b32 v72, v72, s16, 38
	v_min3_f32 v212, v210, v68, v69
	v_and_or_b32 v73, v73, s16, 39
	v_min3_f32 v213, v213, v211, v214
	v_med3_f32 v211, v212, v70, v71
	v_and_or_b32 v74, v74, s16, 40
	v_min3_f32 v210, v212, v70, v71
	v_mfma_f32_32x32x16_f16 v[82:97], v[154:157], v[202:205], v[82:97]
	v_and_or_b32 v75, v75, s16, 41
	v_med3_f32 v214, v210, v72, v73
	v_and_or_b32 v76, v76, s16, 42
	v_min3_f32 v212, v210, v72, v73
	v_and_or_b32 v77, v77, s16, 43
	v_min3_f32 v213, v213, v211, v214
	v_med3_f32 v211, v212, v74, v75
	v_and_or_b32 v78, v78, s16, 44
	v_mfma_f32_32x32x16_f16 v[82:97], v[158:161], v[206:209], v[82:97]
	v_min3_f32 v210, v212, v74, v75
	v_and_or_b32 v79, v79, s16, 45
	v_med3_f32 v214, v210, v76, v77
	v_and_or_b32 v80, v80, s16, 46
	v_min3_f32 v212, v210, v76, v77
	v_and_or_b32 v81, v81, s16, 47
	v_min3_f32 v213, v213, v211, v214
	v_med3_f32 v211, v212, v78, v79
	v_min3_f32 v210, v212, v78, v79
	v_med3_f32 v214, v210, v80, v81
	v_min3_f32 v212, v210, v80, v81
	v_min3_f32 v213, v213, v211, v214
	v_and_or_b32 v82, v82, s16, 48
	v_and_or_b32 v83, v83, s16, 49
	v_and_or_b32 v84, v84, s16, 50
	v_and_or_b32 v85, v85, s16, 51
	v_med3_f32 v211, v212, v82, v83
	v_and_or_b32 v86, v86, s16, 52
	v_min3_f32 v210, v212, v82, v83
	v_and_or_b32 v87, v87, s16, 53
	v_med3_f32 v214, v210, v84, v85
	v_and_or_b32 v88, v88, s16, 54
	v_min3_f32 v212, v210, v84, v85
	v_and_or_b32 v89, v89, s16, 55
	v_min3_f32 v213, v213, v211, v214
	v_med3_f32 v211, v212, v86, v87
	v_and_or_b32 v90, v90, s16, 56
	v_min3_f32 v210, v212, v86, v87
	v_and_or_b32 v91, v91, s16, 57
	v_med3_f32 v214, v210, v88, v89
	v_and_or_b32 v92, v92, s16, 58
	v_min3_f32 v212, v210, v88, v89
	v_and_or_b32 v93, v93, s16, 59
	v_min3_f32 v213, v213, v211, v214
	v_med3_f32 v211, v212, v90, v91
	v_and_or_b32 v94, v94, s16, 60
	v_min3_f32 v210, v212, v90, v91
	v_and_or_b32 v95, v95, s16, 61
	v_med3_f32 v214, v210, v92, v93
	v_and_or_b32 v96, v96, s16, 62
	v_min3_f32 v212, v210, v92, v93
	v_or_b32_e32 v97, 63, v97
	v_min3_f32 v213, v213, v211, v214
	v_med3_f32 v211, v212, v94, v95
	v_min3_f32 v210, v212, v94, v95
	v_med3_f32 v214, v210, v96, v97
	v_min3_f32 v212, v210, v96, v97
	v_min3_f32 v213, v213, v211, v214
	s_and_b32 s0, s17, 1
	s_mulk_i32 s0, 0x1200
	v_add_u32_e32 v254, s0, v177
	ds_write_b64 v254, v[212:213]
	s_branch .LBB0_87
.LBB0_97:
	v_cmp_lt_i32_e64 s[0:1], -1, v192
	s_waitcnt vmcnt(0)
	s_and_saveexec_b64 s[6:7], s[0:1]
	s_cbranch_execz .Low_a_doned
	v_pk_add_f32 v[66:67], v[246:247], v[224:225] neg_lo:[0,1] neg_hi:[0,1]
	v_pk_add_f32 v[74:75], v[248:249], v[226:227] neg_lo:[0,1] neg_hi:[0,1]
	v_pk_fma_f32 v[222:223], v[66:67], v[66:67], v[222:223]
	v_pk_fma_f32 v[222:223], v[74:75], v[74:75], v[222:223]
	v_pk_add_f32 v[66:67], v[224:225], v[66:67]
	v_pk_add_f32 v[68:69], v[226:227], v[74:75]
	global_store_dwordx4 v[168:169], v[66:69], off sc0 sc1
	s_nop 1
